# v3 + one static s_setprio 1 for waves 4-7 before every attention tile loop (GQA, neighbourhood, context), reset at the unit epilogue
# baseline (speedup 1.0000x reference)
.LBB0_703:
	s_andn2_b64 vcc, exec, s[0:1]
	s_cbranch_vccnz .LBB0_907
	s_add_i32 s0, s35, 7
	v_add_u32_e32 v0, s2, v4
	s_and_b32 s12, s0, -4
	v_med3_u32 v1, v0, 8, 56
	s_bfe_u32 s0, s33, 0x60019
	s_add_i32 s0, s33, s0
	v_sub_u32_e32 v1, v209, v1
	s_sext_i32_i16 s0, s0
	v_add_u32_e32 v2, 8, v1
	s_ashr_i32 s10, s0, 6
	v_cmp_gt_u32_e64 s[0:1], 16, v2
	v_mad_u32_u24 v210, v4, s58, 0
	v_lshlrev_b32_e32 v3, 3, v4
	v_writelane_b32 v255, s0, 6
	v_sub_u32_e32 v211, v210, v3
	v_and_b32_e32 v3, -16, v2
	v_writelane_b32 v255, s1, 7
	s_movk_i32 s0, 0xffe0
	v_cmp_eq_u32_e64 s[42:43], s0, v3
	v_add_u32_e32 v4, 9, v1
	s_movk_i32 s0, 0xffef
	v_cmp_gt_u32_e64 s[44:45], 16, v4
	v_add_u32_e32 v4, 41, v1
	v_cmp_lt_u32_e64 s[72:73], s0, v2
	v_add_u32_e32 v2, 25, v1
	v_cmp_gt_u32_e64 s[46:47], 16, v4
	v_add_u32_e32 v4, 10, v1
	v_cmp_gt_u32_e64 s[76:77], 16, v2
	v_add_u32_e32 v2, 57, v1
	v_cmp_gt_u32_e64 s[48:49], 16, v4
	v_add_u32_e32 v4, 42, v1
	v_cmp_gt_u32_e64 s[78:79], 16, v2
	v_add_u32_e32 v2, 26, v1
	v_cmp_gt_u32_e64 s[50:51], 16, v4
	v_add_u32_e32 v4, 11, v1
	v_cmp_gt_u32_e64 s[80:81], 16, v2
	v_add_u32_e32 v2, 58, v1
	v_cmp_gt_u32_e64 s[52:53], 16, v4
	v_add_u32_e32 v4, 43, v1
	v_cmp_gt_u32_e64 s[82:83], 16, v2
	v_add_u32_e32 v2, 27, v1
	v_cmp_gt_u32_e64 s[54:55], 16, v4
	v_add_u32_e32 v4, 16, v1
	v_cmp_gt_u32_e64 s[84:85], 16, v2
	v_add_u32_e32 v2, 59, v1
	v_cmp_gt_u32_e64 s[56:57], 16, v4
	v_add_u32_e32 v4, 48, v1
	v_cmp_gt_u32_e64 s[86:87], 16, v2
	v_add_u32_e32 v2, 32, v1
	v_cmp_gt_u32_e64 s[58:59], 16, v4
	v_add_u32_e32 v4, 17, v1
	v_cmp_gt_u32_e64 s[88:89], 16, v2
	v_add_u32_e32 v2, 64, v1
	v_cmp_gt_u32_e64 s[60:61], 16, v4
	v_add_u32_e32 v4, 49, v1
	v_cmp_gt_u32_e64 s[90:91], 16, v2
	v_add_u32_e32 v2, 33, v1
	v_cmp_gt_u32_e64 s[62:63], 16, v4
	v_add_u32_e32 v4, 18, v1
	v_cmp_gt_u32_e64 s[92:93], 16, v2
	v_add_u32_e32 v2, 0x41, v1
	v_cmp_gt_u32_e64 s[64:65], 16, v4
	v_add_u32_e32 v4, 50, v1
	v_cmp_gt_u32_e64 s[94:95], 16, v2
	v_add_u32_e32 v2, 34, v1
	v_cmp_gt_u32_e64 s[66:67], 16, v4
	v_add_u32_e32 v4, 19, v1
	v_cmp_gt_u32_e64 s[96:97], 16, v2
	v_add_u32_e32 v2, 0x42, v1
	s_mulk_i32 s10, 0x7c
	v_lshlrev_b32_e32 v0, 2, v0
	v_cmp_gt_u32_e64 s[68:69], 16, v4
	v_add_u32_e32 v4, 51, v1
	s_movk_i32 s0, 0xffd0
	v_cmp_gt_u32_e64 s[4:5], 16, v2
	v_add_u32_e32 v2, 35, v1
	v_add_u32_e32 v1, 0x43, v1
	v_sub_u32_e32 v0, s10, v0
	s_mul_i32 s10, s14, 0x7c
	v_mov_b32_e32 v32, v193
	v_mov_b32_e32 v33, v193
	v_cmp_gt_u32_e64 s[70:71], 16, v4
	v_cmp_eq_u32_e64 s[74:75], s0, v3
	v_cmp_gt_u32_e64 s[6:7], 16, v2
	v_cmp_gt_u32_e64 s[8:9], 16, v1
	v_subrev_u32_e32 v213, s10, v0
	v_readlane_b32 s10, v254, 25
	v_mov_b32_e32 v34, v193
	v_mov_b32_e32 v35, v193
	v_mov_b32_e32 v36, v193
	v_mov_b32_e32 v37, v193
	v_mov_b32_e32 v38, v193
	v_mov_b32_e32 v39, v193
	v_mov_b32_e32 v40, v193
	v_mov_b32_e32 v41, v193
	v_mov_b32_e32 v42, v193
	v_mov_b32_e32 v43, v193
	v_mov_b32_e32 v44, v193
	v_mov_b32_e32 v45, v193
	v_mov_b32_e32 v46, v193
	v_mov_b32_e32 v47, v193
	v_mov_b64_e32 v[0:1], v[32:33]
	v_mov_b64_e32 v[16:17], v[32:33]
	s_add_i32 s28, s35, 4
	s_add_i32 s2, s21, 7
	s_mov_b64 s[16:17], -1
	s_xor_b64 s[0:1], s[36:37], -1
	v_add_u32_e32 v214, s10, v208
	s_mov_b32 s29, 0
	v_mov_b32_e32 v212, 0
	v_mov_b32_e32 v215, 0
	v_mov_b64_e32 v[2:3], v[34:35]
	v_mov_b64_e32 v[4:5], v[36:37]
	v_mov_b64_e32 v[6:7], v[38:39]
	v_mov_b64_e32 v[8:9], v[40:41]
	v_mov_b64_e32 v[10:11], v[42:43]
	v_mov_b64_e32 v[12:13], v[44:45]
	v_mov_b64_e32 v[14:15], v[46:47]
	v_mov_b64_e32 v[18:19], v[34:35]
	v_mov_b64_e32 v[20:21], v[36:37]
	v_mov_b64_e32 v[22:23], v[38:39]
	v_mov_b64_e32 v[24:25], v[40:41]
	v_mov_b64_e32 v[26:27], v[42:43]
	v_mov_b64_e32 v[28:29], v[44:45]
	v_mov_b64_e32 v[30:31], v[46:47]
	v_readlane_b32 s10, v252, 6
	s_cmp_lt_u32 s10, 0x100
	s_cbranch_scc1 .Lat_noprio
	s_setprio 1
.Lat_noprio:
	s_cmp_eq_u32 s35, 64
	s_cbranch_scc1 .Lfa_entry

.LBB0_908:
	s_setprio 0
	v_readlane_b32 s84, v254, 44
	v_mov_b32_e32 v32, v209
	v_readlane_b32 s85, v254, 45
	s_movk_i32 s58, 0x90
	s_movk_i32 s59, 0xffd0
